# P10: cooperative L2 prefetch two units deep (k-tiles 2,3 of unit u+1 and k-tiles 0,1 of unit u+2 from unit u's epilogue)
# baseline (speedup 1.0000x reference)
.LBB0_1446:
	v_readfirstlane_b32 s70, v0
	s_lshr_b32 s70, s70, 6
	s_add_i32 s71, s53, 1
	s_mul_i32 s71, s71, s52
	s_add_i32 s71, s71, s33
	s_lshr_b32 s72, s71, 3
	s_add_i32 s72, s72, s42
	s_cmp_lt_i32 s72, s43
	s_cselect_b32 s72, s72, s66
	v_mov_b32_e32 v249, s72
	v_add_u32_e32 v249, 0x24800, v249
	ds_read_u8 v249, v249
	s_cmp_eq_u64 s[2:3], 0
	s_cselect_b32 s71, s65, s66
	s_and_b32 s75, s70, 1
	s_lshl_b32 s73, s28, 14
	s_cmp_eq_u32 s75, 0
	s_cselect_b32 s74, s71, s72
	s_cselect_b32 s76, 0x100, 0
	s_lshl_b32 s74, s74, 17
	s_add_u32 s74, s74, s73
	s_add_u32 s74, s74, s76
	s_add_u32 s76, s12, s74
	s_addc_u32 s77, s13, 0
	s_bfe_u32 s74, s80, 0x20006
	s_lshl_b32 s74, s74, 15
	s_lshl_b32 s78, s75, 14
	s_add_u32 s74, s74, s78
	s_waitcnt lgkmcnt(0)
	v_readfirstlane_b32 s78, v249
	s_lshl_b32 s78, s78, 20
	s_lshl_b32 s79, s28, 17
	s_add_u32 s78, s78, s79
	s_add_u32 s78, s78, s74
	s_add_u32 s78, s44, s78
	s_addc_u32 s79, s45, 0
	s_add_u32 s74, s74, 0x100
	s_add_u32 s74, s26, s74
	s_addc_u32 s75, s27, 0
	s_lshr_b32 s71, s70, 1
	s_cmp_eq_u32 s71, 1
	s_cselect_b64 s[76:77], s[74:75], s[76:77]
	s_cmp_eq_u32 s71, 2
	s_cselect_b64 s[76:77], s[78:79], s[76:77]
	v_lshrrev_b32_e32 v250, 1, v206
	v_and_b32_e32 v249, 1, v206
	v_lshlrev_b32_e32 v250, 9, v250
	v_lshl_or_b32 v250, v249, 7, v250
	global_load_dword v251, v250, s[76:77]
	v_lshl_or_b32 v10, s28, 8, v190
	v_max_f32_e32 v2, v158, v158
	v_med3_f32 v3, v2, s64, v196
	v_max_f32_e32 v2, v159, v159
	v_med3_f32 v4, v2, s64, v196
	v_mov_b32_e32 v2, v169
	v_cvt_pk_fp8_f32 v2, v3, v4
	v_max_f32_e32 v5, v160, v160
	v_max_f32_e32 v4, v161, v161
	v_med3_f32 v3, v5, s64, v196
	v_med3_f32 v4, v4, s64, v196
	v_cvt_pk_fp8_f32 v2, v3, v4 op_sel:[0,0,1]
	v_max_f32_e32 v3, v154, v154
	v_med3_f32 v4, v3, s64, v196
	v_max_f32_e32 v3, v155, v155
	v_med3_f32 v5, v3, s64, v196
	v_mov_b32_e32 v3, v169
	v_cvt_pk_fp8_f32 v3, v4, v5
	v_max_f32_e32 v6, v156, v156
	v_max_f32_e32 v5, v157, v157
	v_med3_f32 v4, v6, s64, v196
	v_med3_f32 v5, v5, s64, v196
	v_cvt_pk_fp8_f32 v3, v4, v5 op_sel:[0,0,1]
	v_max_f32_e32 v4, v150, v150
	v_med3_f32 v5, v4, s64, v196
	v_max_f32_e32 v4, v151, v151
	v_med3_f32 v6, v4, s64, v196
	v_mov_b32_e32 v4, v169
	v_cvt_pk_fp8_f32 v4, v5, v6
	v_max_f32_e32 v7, v152, v152
	v_max_f32_e32 v6, v153, v153
	v_med3_f32 v5, v7, s64, v196
	v_med3_f32 v6, v6, s64, v196
	v_cvt_pk_fp8_f32 v4, v5, v6 op_sel:[0,0,1]
	v_max_f32_e32 v5, v146, v146
	v_med3_f32 v6, v5, s64, v196
	v_max_f32_e32 v5, v147, v147
	v_med3_f32 v7, v5, s64, v196
	v_mov_b32_e32 v5, v169
	v_cvt_pk_fp8_f32 v5, v6, v7
	v_max_f32_e32 v8, v148, v148
	v_max_f32_e32 v7, v149, v149
	v_med3_f32 v6, v8, s64, v196
	v_med3_f32 v7, v7, s64, v196
	v_cvt_pk_fp8_f32 v5, v6, v7 op_sel:[0,0,1]
	v_max_f32_e32 v6, v142, v142
	v_med3_f32 v7, v6, s64, v196
	v_max_f32_e32 v6, v143, v143
	v_med3_f32 v8, v6, s64, v196
	v_mov_b32_e32 v6, v169
	v_cvt_pk_fp8_f32 v6, v7, v8
	v_max_f32_e32 v9, v144, v144
	v_max_f32_e32 v8, v145, v145
	v_med3_f32 v7, v9, s64, v196
	v_med3_f32 v8, v8, s64, v196
	v_cvt_pk_fp8_f32 v6, v7, v8 op_sel:[0,0,1]
	v_max_f32_e32 v7, v138, v138
	v_med3_f32 v8, v7, s64, v196
	v_max_f32_e32 v7, v139, v139
	v_med3_f32 v9, v7, s64, v196
	v_mov_b32_e32 v7, v169
	v_cvt_pk_fp8_f32 v7, v8, v9
	v_max_f32_e32 v11, v140, v140
	v_max_f32_e32 v9, v141, v141
	v_med3_f32 v8, v11, s64, v196
	v_med3_f32 v9, v9, s64, v196
	v_cvt_pk_fp8_f32 v7, v8, v9 op_sel:[0,0,1]
	v_max_f32_e32 v8, v134, v134
	v_med3_f32 v9, v8, s64, v196
	v_max_f32_e32 v8, v135, v135
	v_med3_f32 v11, v8, s64, v196
	v_mov_b32_e32 v8, v169
	v_cvt_pk_fp8_f32 v8, v9, v11
	v_max_f32_e32 v12, v136, v136
	v_max_f32_e32 v11, v137, v137
	v_med3_f32 v9, v12, s64, v196
	v_med3_f32 v11, v11, s64, v196
	v_cvt_pk_fp8_f32 v8, v9, v11 op_sel:[0,0,1]
	v_max_f32_e32 v9, v130, v130
	v_med3_f32 v11, v9, s64, v196
	v_max_f32_e32 v9, v131, v131
	v_med3_f32 v12, v9, s64, v196
	v_mov_b32_e32 v9, v169
	v_cvt_pk_fp8_f32 v9, v11, v12
	v_max_f32_e32 v13, v132, v132
	v_max_f32_e32 v12, v133, v133
	v_med3_f32 v11, v13, s64, v196
	v_med3_f32 v12, v12, s64, v196
	v_cvt_pk_fp8_f32 v9, v11, v12 op_sel:[0,0,1]
	s_lshl_b32 s23, s66, 19
	v_add3_u32 v10, s23, v171, v10
	buffer_store_dwordx4 v[2:5], v10, s[4:7], 0 offen
	v_max_f32_e32 v11, v108, v108
	v_max_f32_e32 v12, v104, v104
	v_add_u32_e32 v2, 0x8000, v10
	buffer_store_dwordx4 v[6:9], v2, s[4:7], 0 offen
	v_max_f32_e32 v2, v126, v126
	v_med3_f32 v3, v2, s64, v196
	v_max_f32_e32 v2, v127, v127
	v_med3_f32 v4, v2, s64, v196
	v_mov_b32_e32 v2, v169
	v_cvt_pk_fp8_f32 v2, v3, v4
	v_max_f32_e32 v5, v128, v128
	v_max_f32_e32 v4, v129, v129
	v_med3_f32 v3, v5, s64, v196
	v_med3_f32 v4, v4, s64, v196
	v_cvt_pk_fp8_f32 v2, v3, v4 op_sel:[0,0,1]
	v_max_f32_e32 v3, v122, v122
	v_med3_f32 v4, v3, s64, v196
	v_max_f32_e32 v3, v123, v123
	v_med3_f32 v5, v3, s64, v196
	v_mov_b32_e32 v3, v169
	v_cvt_pk_fp8_f32 v3, v4, v5
	v_max_f32_e32 v6, v124, v124
	v_max_f32_e32 v5, v125, v125
	v_med3_f32 v4, v6, s64, v196
	v_med3_f32 v5, v5, s64, v196
	v_cvt_pk_fp8_f32 v3, v4, v5 op_sel:[0,0,1]
	v_max_f32_e32 v4, v118, v118
	v_med3_f32 v5, v4, s64, v196
	v_max_f32_e32 v4, v119, v119
	v_med3_f32 v6, v4, s64, v196
	v_mov_b32_e32 v4, v169
	v_cvt_pk_fp8_f32 v4, v5, v6
	v_max_f32_e32 v7, v120, v120
	v_max_f32_e32 v6, v121, v121
	v_med3_f32 v5, v7, s64, v196
	v_med3_f32 v6, v6, s64, v196
	v_cvt_pk_fp8_f32 v4, v5, v6 op_sel:[0,0,1]
	v_max_f32_e32 v5, v114, v114
	v_med3_f32 v6, v5, s64, v196
	v_max_f32_e32 v5, v115, v115
	v_med3_f32 v7, v5, s64, v196
	v_mov_b32_e32 v5, v169
	v_cvt_pk_fp8_f32 v5, v6, v7
	v_max_f32_e32 v8, v116, v116
	v_max_f32_e32 v7, v117, v117
	v_med3_f32 v6, v8, s64, v196
	v_med3_f32 v7, v7, s64, v196
	v_cvt_pk_fp8_f32 v5, v6, v7 op_sel:[0,0,1]
	v_max_f32_e32 v6, v110, v110
	v_med3_f32 v7, v6, s64, v196
	v_max_f32_e32 v6, v111, v111
	v_med3_f32 v8, v6, s64, v196
	v_mov_b32_e32 v6, v169
	v_cvt_pk_fp8_f32 v6, v7, v8
	v_max_f32_e32 v9, v112, v112
	v_max_f32_e32 v8, v113, v113
	v_med3_f32 v7, v9, s64, v196
	v_med3_f32 v8, v8, s64, v196
	v_cvt_pk_fp8_f32 v6, v7, v8 op_sel:[0,0,1]
	v_max_f32_e32 v7, v106, v106
	v_med3_f32 v8, v7, s64, v196
	v_max_f32_e32 v7, v107, v107
	v_med3_f32 v9, v7, s64, v196
	v_mov_b32_e32 v7, v169
	v_cvt_pk_fp8_f32 v7, v8, v9
	v_max_f32_e32 v9, v109, v109
	v_med3_f32 v8, v11, s64, v196
	v_med3_f32 v9, v9, s64, v196
	v_cvt_pk_fp8_f32 v7, v8, v9 op_sel:[0,0,1]
	v_max_f32_e32 v8, v102, v102
	v_med3_f32 v9, v8, s64, v196
	v_max_f32_e32 v8, v103, v103
	v_med3_f32 v11, v8, s64, v196
	v_mov_b32_e32 v8, v169
	v_cvt_pk_fp8_f32 v8, v9, v11
	v_max_f32_e32 v11, v105, v105
	v_med3_f32 v9, v12, s64, v196
	v_med3_f32 v11, v11, s64, v196
	v_cvt_pk_fp8_f32 v8, v9, v11 op_sel:[0,0,1]
	v_max_f32_e32 v9, v98, v98
	v_med3_f32 v11, v9, s64, v196
	v_max_f32_e32 v9, v99, v99
	v_med3_f32 v12, v9, s64, v196
	v_mov_b32_e32 v9, v169
	v_cvt_pk_fp8_f32 v9, v11, v12
	v_max_f32_e32 v13, v100, v100
	v_max_f32_e32 v12, v101, v101
	v_med3_f32 v11, v13, s64, v196
	v_med3_f32 v12, v12, s64, v196
	v_cvt_pk_fp8_f32 v9, v11, v12 op_sel:[0,0,1]
	v_add_u32_e32 v11, 0x10000, v10
	buffer_store_dwordx4 v[2:5], v11, s[4:7], 0 offen
	v_max_f32_e32 v11, v76, v76
	v_max_f32_e32 v12, v72, v72
	v_add_u32_e32 v2, 0x18000, v10
	buffer_store_dwordx4 v[6:9], v2, s[4:7], 0 offen
	v_max_f32_e32 v2, v94, v94
	v_med3_f32 v3, v2, s64, v196
	v_max_f32_e32 v2, v95, v95
	v_med3_f32 v4, v2, s64, v196
	v_mov_b32_e32 v2, v169
	v_cvt_pk_fp8_f32 v2, v3, v4
	v_max_f32_e32 v5, v96, v96
	v_max_f32_e32 v4, v97, v97
	v_med3_f32 v3, v5, s64, v196
	v_med3_f32 v4, v4, s64, v196
	v_cvt_pk_fp8_f32 v2, v3, v4 op_sel:[0,0,1]
	v_max_f32_e32 v3, v90, v90
	v_med3_f32 v4, v3, s64, v196
	v_max_f32_e32 v3, v91, v91
	v_med3_f32 v5, v3, s64, v196
	v_mov_b32_e32 v3, v169
	v_cvt_pk_fp8_f32 v3, v4, v5
	v_max_f32_e32 v6, v92, v92
	v_max_f32_e32 v5, v93, v93
	v_med3_f32 v4, v6, s64, v196
	v_med3_f32 v5, v5, s64, v196
	v_cvt_pk_fp8_f32 v3, v4, v5 op_sel:[0,0,1]
	v_max_f32_e32 v4, v86, v86
	v_med3_f32 v5, v4, s64, v196
	v_max_f32_e32 v4, v87, v87
	v_med3_f32 v6, v4, s64, v196
	v_mov_b32_e32 v4, v169
	v_cvt_pk_fp8_f32 v4, v5, v6
	v_max_f32_e32 v7, v88, v88
	v_max_f32_e32 v6, v89, v89
	v_med3_f32 v5, v7, s64, v196
	v_med3_f32 v6, v6, s64, v196
	v_cvt_pk_fp8_f32 v4, v5, v6 op_sel:[0,0,1]
	v_max_f32_e32 v5, v82, v82
	v_med3_f32 v6, v5, s64, v196
	v_max_f32_e32 v5, v83, v83
	v_med3_f32 v7, v5, s64, v196
	v_mov_b32_e32 v5, v169
	v_cvt_pk_fp8_f32 v5, v6, v7
	v_max_f32_e32 v8, v84, v84
	v_max_f32_e32 v7, v85, v85
	v_med3_f32 v6, v8, s64, v196
	v_med3_f32 v7, v7, s64, v196
	v_cvt_pk_fp8_f32 v5, v6, v7 op_sel:[0,0,1]
	v_max_f32_e32 v6, v78, v78
	v_med3_f32 v7, v6, s64, v196
	v_max_f32_e32 v6, v79, v79
	v_med3_f32 v8, v6, s64, v196
	v_mov_b32_e32 v6, v169
	v_cvt_pk_fp8_f32 v6, v7, v8
	v_max_f32_e32 v9, v80, v80
	v_max_f32_e32 v8, v81, v81
	v_med3_f32 v7, v9, s64, v196
	v_med3_f32 v8, v8, s64, v196
	v_cvt_pk_fp8_f32 v6, v7, v8 op_sel:[0,0,1]
	v_max_f32_e32 v7, v74, v74
	v_med3_f32 v8, v7, s64, v196
	v_max_f32_e32 v7, v75, v75
	v_med3_f32 v9, v7, s64, v196
	v_mov_b32_e32 v7, v169
	v_cvt_pk_fp8_f32 v7, v8, v9
	v_max_f32_e32 v9, v77, v77
	v_med3_f32 v8, v11, s64, v196
	v_med3_f32 v9, v9, s64, v196
	v_cvt_pk_fp8_f32 v7, v8, v9 op_sel:[0,0,1]
	v_max_f32_e32 v8, v70, v70
	v_med3_f32 v9, v8, s64, v196
	v_max_f32_e32 v8, v71, v71
	v_med3_f32 v11, v8, s64, v196
	v_mov_b32_e32 v8, v169
	v_cvt_pk_fp8_f32 v8, v9, v11
	v_max_f32_e32 v11, v73, v73
	v_med3_f32 v9, v12, s64, v196
	v_med3_f32 v11, v11, s64, v196
	v_cvt_pk_fp8_f32 v8, v9, v11 op_sel:[0,0,1]
	v_max_f32_e32 v9, v66, v66
	v_med3_f32 v11, v9, s64, v196
	v_max_f32_e32 v9, v67, v67
	v_med3_f32 v12, v9, s64, v196
	v_mov_b32_e32 v9, v169
	v_cvt_pk_fp8_f32 v9, v11, v12
	v_max_f32_e32 v13, v68, v68
	v_max_f32_e32 v12, v69, v69
	v_med3_f32 v11, v13, s64, v196
	v_med3_f32 v12, v12, s64, v196
	v_cvt_pk_fp8_f32 v9, v11, v12 op_sel:[0,0,1]
	v_add_u32_e32 v11, 0x40000, v10
	buffer_store_dwordx4 v[2:5], v11, s[4:7], 0 offen
	v_max_f32_e32 v11, v44, v44
	v_max_f32_e32 v12, v40, v40
	v_add_u32_e32 v2, 0x48000, v10
	buffer_store_dwordx4 v[6:9], v2, s[4:7], 0 offen
	v_max_f32_e32 v2, v62, v62
	v_med3_f32 v3, v2, s64, v196
	v_max_f32_e32 v2, v63, v63
	v_med3_f32 v4, v2, s64, v196
	v_mov_b32_e32 v2, v169
	v_cvt_pk_fp8_f32 v2, v3, v4
	v_max_f32_e32 v5, v64, v64
	v_max_f32_e32 v4, v65, v65
	v_med3_f32 v3, v5, s64, v196
	v_med3_f32 v4, v4, s64, v196
	v_cvt_pk_fp8_f32 v2, v3, v4 op_sel:[0,0,1]
	v_max_f32_e32 v3, v58, v58
	v_med3_f32 v4, v3, s64, v196
	v_max_f32_e32 v3, v59, v59
	v_med3_f32 v5, v3, s64, v196
	v_mov_b32_e32 v3, v169
	v_cvt_pk_fp8_f32 v3, v4, v5
	v_max_f32_e32 v6, v60, v60
	v_max_f32_e32 v5, v61, v61
	v_med3_f32 v4, v6, s64, v196
	v_med3_f32 v5, v5, s64, v196
	v_cvt_pk_fp8_f32 v3, v4, v5 op_sel:[0,0,1]
	v_max_f32_e32 v4, v54, v54
	v_med3_f32 v5, v4, s64, v196
	v_max_f32_e32 v4, v55, v55
	v_med3_f32 v6, v4, s64, v196
	v_mov_b32_e32 v4, v169
	v_cvt_pk_fp8_f32 v4, v5, v6
	v_max_f32_e32 v7, v56, v56
	v_max_f32_e32 v6, v57, v57
	v_med3_f32 v5, v7, s64, v196
	v_med3_f32 v6, v6, s64, v196
	v_cvt_pk_fp8_f32 v4, v5, v6 op_sel:[0,0,1]
	v_max_f32_e32 v5, v50, v50
	v_med3_f32 v6, v5, s64, v196
	v_max_f32_e32 v5, v51, v51
	v_med3_f32 v7, v5, s64, v196
	v_mov_b32_e32 v5, v169
	v_cvt_pk_fp8_f32 v5, v6, v7
	v_max_f32_e32 v8, v52, v52
	v_max_f32_e32 v7, v53, v53
	v_med3_f32 v6, v8, s64, v196
	v_med3_f32 v7, v7, s64, v196
	v_cvt_pk_fp8_f32 v5, v6, v7 op_sel:[0,0,1]
	v_max_f32_e32 v6, v46, v46
	v_med3_f32 v7, v6, s64, v196
	v_max_f32_e32 v6, v47, v47
	v_med3_f32 v8, v6, s64, v196
	v_mov_b32_e32 v6, v169
	v_cvt_pk_fp8_f32 v6, v7, v8
	v_max_f32_e32 v9, v48, v48
	v_max_f32_e32 v8, v49, v49
	v_med3_f32 v7, v9, s64, v196
	v_med3_f32 v8, v8, s64, v196
	v_cvt_pk_fp8_f32 v6, v7, v8 op_sel:[0,0,1]
	v_max_f32_e32 v7, v42, v42
	v_med3_f32 v8, v7, s64, v196
	v_max_f32_e32 v7, v43, v43
	v_med3_f32 v9, v7, s64, v196
	v_mov_b32_e32 v7, v169
	v_cvt_pk_fp8_f32 v7, v8, v9
	v_max_f32_e32 v9, v45, v45
	v_med3_f32 v8, v11, s64, v196
	v_med3_f32 v9, v9, s64, v196
	v_cvt_pk_fp8_f32 v7, v8, v9 op_sel:[0,0,1]
	v_max_f32_e32 v8, v38, v38
	v_med3_f32 v9, v8, s64, v196
	v_max_f32_e32 v8, v39, v39
	v_med3_f32 v11, v8, s64, v196
	v_mov_b32_e32 v8, v169
	v_cvt_pk_fp8_f32 v8, v9, v11
	v_max_f32_e32 v11, v41, v41
	v_med3_f32 v9, v12, s64, v196
	v_med3_f32 v11, v11, s64, v196
	v_cvt_pk_fp8_f32 v8, v9, v11 op_sel:[0,0,1]
	v_max_f32_e32 v9, v34, v34
	v_med3_f32 v11, v9, s64, v196
	v_max_f32_e32 v9, v35, v35
	v_med3_f32 v12, v9, s64, v196
	v_mov_b32_e32 v9, v169
	v_cvt_pk_fp8_f32 v9, v11, v12
	v_max_f32_e32 v13, v36, v36
	v_max_f32_e32 v12, v37, v37
	v_med3_f32 v11, v13, s64, v196
	v_med3_f32 v12, v12, s64, v196
	v_cvt_pk_fp8_f32 v9, v11, v12 op_sel:[0,0,1]
	v_add_u32_e32 v11, 0x50000, v10
	buffer_store_dwordx4 v[2:5], v11, s[4:7], 0 offen
	s_and_b64 vcc, exec, s[2:3]
	s_mov_b64 s[2:3], -1
	v_add_u32_e32 v2, 0x58000, v10
	buffer_store_dwordx4 v[6:9], v2, s[4:7], 0 offen
	s_mov_b32 s98, 1
	s_cbranch_vccnz .LBB0_1436
	s_andn2_b64 vcc, exec, s[14:15]
	s_cbranch_vccnz .LBB0_1435
	s_barrier
	s_branch .LBB0_1435
